# baseline (speedup 1.0000x reference)
.Lm_norescale1:
	v_exp_f32_e32 v234, v74
	v_exp_f32_e32 v235, v75
	v_exp_f32_e32 v236, v76
	v_exp_f32_e32 v237, v77
	v_exp_f32_e32 v238, v78
	v_exp_f32_e32 v239, v79
	v_exp_f32_e32 v240, v80
	v_exp_f32_e32 v241, v81
	v_exp_f32_e32 v106, v82
	v_exp_f32_e32 v107, v83
	v_exp_f32_e32 v108, v84
	v_exp_f32_e32 v109, v85
	v_exp_f32_e32 v110, v86
	v_exp_f32_e32 v111, v87
	v_exp_f32_e32 v112, v88
	v_exp_f32_e32 v113, v89
	s_setprio 1
	v_pk_add_f32 v[18:19], v[234:235], v[18:19]
	v_pk_add_f32 v[20:21], v[236:237], v[20:21]
	v_pk_add_f32 v[22:23], v[238:239], v[22:23]
	v_pk_add_f32 v[24:25], v[240:241], v[24:25]
	v_pk_add_f32 v[26:27], v[106:107], v[26:27]
	v_pk_add_f32 v[28:29], v[108:109], v[28:29]
	v_pk_add_f32 v[30:31], v[110:111], v[30:31]
	v_pk_add_f32 v[32:33], v[112:113], v[32:33]
	v_fma_mix_f32 v206, v234, v122, v206 op_sel:[0,0,0] op_sel_hi:[0,1,0]
	v_fma_mix_f32 v207, v235, v122, v207 op_sel:[0,1,0] op_sel_hi:[0,1,0]
	v_fma_mix_f32 v200, v236, v123, v200 op_sel:[0,0,0] op_sel_hi:[0,1,0]
	v_fma_mix_f32 v201, v237, v123, v201 op_sel:[0,1,0] op_sel_hi:[0,1,0]
	v_fma_mix_f32 v198, v238, v124, v198 op_sel:[0,0,0] op_sel_hi:[0,1,0]
	v_fma_mix_f32 v199, v239, v124, v199 op_sel:[0,1,0] op_sel_hi:[0,1,0]
	v_fma_mix_f32 v194, v240, v125, v194 op_sel:[0,0,0] op_sel_hi:[0,1,0]
	v_fma_mix_f32 v195, v241, v125, v195 op_sel:[0,1,0] op_sel_hi:[0,1,0]
	v_fma_mix_f32 v192, v106, v182, v192 op_sel:[0,0,0] op_sel_hi:[0,1,0]
	v_fma_mix_f32 v193, v107, v182, v193 op_sel:[0,1,0] op_sel_hi:[0,1,0]
	v_fma_mix_f32 v190, v108, v183, v190 op_sel:[0,0,0] op_sel_hi:[0,1,0]
	v_fma_mix_f32 v191, v109, v183, v191 op_sel:[0,1,0] op_sel_hi:[0,1,0]
	v_fma_mix_f32 v188, v110, v184, v188 op_sel:[0,0,0] op_sel_hi:[0,1,0]
	v_fma_mix_f32 v189, v111, v184, v189 op_sel:[0,1,0] op_sel_hi:[0,1,0]
	v_fma_mix_f32 v186, v112, v185, v186 op_sel:[0,0,0] op_sel_hi:[0,1,0]
	v_fma_mix_f32 v187, v113, v185, v187 op_sel:[0,1,0] op_sel_hi:[0,1,0]
	s_addk_i32 s4, 0x280
	s_cmpk_eq_i32 s4, 0x2080
	s_cbranch_scc0 .LBB1_14
	s_waitcnt lgkmcnt(0)
